# GEMM K-loops: non-scaled v_mfma_f32_16x16x128_f8f6f4 (same e4m3 operands, unit scale was 2^0) instead of the scale form with its ld_scale prefix
# speedup vs baseline: 1.0099x; 1.0065x over previous
.LBB0_247:
	s_add_u32 s50, s48, 0x80
	s_addc_u32 s51, s49, 0
	s_add_i32 s74, 0, 0x10000
	v_add_u32_e32 v220, s74, v147
	v_add_u32_e32 v221, s74, v148
	ds_read_b128 v[222:225], v220
	ds_read_b128 v[230:233], v220 offset:2048
	ds_read_b128 v[226:229], v221
	ds_read_b128 v[234:237], v221 offset:2048
	s_cmp_eq_u32 s73, 12
	s_cselect_b32 s53, s5, s51
	s_cselect_b32 s52, s43, s50
	s_cselect_b32 s51, s8, s72
	s_cselect_b32 s50, s9, s67
	s_add_i32 s75, s31, s55
	v_lshl_add_u64 v[142:143], s[48:49], 0, v[140:141]
	s_mov_b32 m0, s75
	ds_read_b128 v[168:171], v150
	ds_read_b128 v[182:185], v150 offset:2048
	ds_read_b128 v[172:175], v151
	ds_read_b128 v[186:189], v151 offset:2048
	ds_read_b128 v[190:193], v150 offset:4096
	ds_read_b128 v[198:201], v150 offset:6144
	ds_read_b128 v[194:197], v151 offset:4096
	ds_read_b128 v[202:205], v151 offset:6144
	global_load_lds_dwordx4 v[142:143], off
	v_lshl_add_u64 v[142:143], s[48:49], 0, v[138:139]
	s_add_i32 m0, s75, 0x2000
	s_nop 0
	global_load_lds_dwordx4 v[142:143], off
	s_waitcnt vmcnt(6)
	s_waitcnt lgkmcnt(0)
	s_barrier
	s_setprio 1
	s_waitcnt lgkmcnt(0)
	v_mfma_f32_16x16x128_f8f6f4 v[128:131], v[222:229], v[168:175], v[128:131]
	v_mfma_f32_16x16x128_f8f6f4 v[124:127], v[230:237], v[168:175], v[124:127]
	v_mfma_f32_16x16x128_f8f6f4 v[120:123], v[222:229], v[182:189], v[120:123]
	v_mfma_f32_16x16x128_f8f6f4 v[112:115], v[230:237], v[182:189], v[112:115]
	v_mfma_f32_16x16x128_f8f6f4 v[104:107], v[222:229], v[190:197], v[104:107]
	v_mfma_f32_16x16x128_f8f6f4 v[96:99], v[230:237], v[190:197], v[96:99]
	v_mfma_f32_16x16x128_f8f6f4 v[88:91], v[222:229], v[198:205], v[88:91]
	v_mfma_f32_16x16x128_f8f6f4 v[80:83], v[230:237], v[198:205], v[80:83]
	s_setprio 0
	s_barrier
	s_add_i32 s75, 0, 0x14000
	v_add_u32_e32 v142, s75, v147
	v_add_u32_e32 v143, s75, v148
	s_mov_b32 m0, s56
	ds_read_b128 v[152:155], v142
	ds_read_b128 v[160:163], v142 offset:2048
	ds_read_b128 v[156:159], v143
	ds_read_b128 v[164:167], v143 offset:2048
	v_lshl_add_u64 v[142:143], s[50:51], 0, v[2:3]
	global_load_lds_dwordx4 v[142:143], off
	v_lshl_add_u64 v[144:145], s[50:51], 0, v[134:135]
	s_mov_b32 m0, s57
	s_nop 0
	global_load_lds_dwordx4 v[144:145], off
	s_waitcnt vmcnt(6)
	s_waitcnt lgkmcnt(0)
	s_barrier
	s_setprio 1
	s_waitcnt lgkmcnt(0)
	v_mfma_f32_16x16x128_f8f6f4 v[116:119], v[152:159], v[168:175], v[116:119]
	v_mfma_f32_16x16x128_f8f6f4 v[108:111], v[160:167], v[168:175], v[108:111]
	v_mfma_f32_16x16x128_f8f6f4 v[100:103], v[152:159], v[182:189], v[100:103]
	v_mfma_f32_16x16x128_f8f6f4 v[92:95], v[160:167], v[182:189], v[92:95]
	v_mfma_f32_16x16x128_f8f6f4 v[84:87], v[152:159], v[190:197], v[84:87]
	v_mfma_f32_16x16x128_f8f6f4 v[76:79], v[160:167], v[190:197], v[76:79]
	v_mfma_f32_16x16x128_f8f6f4 v[72:75], v[152:159], v[198:205], v[72:75]
	v_mfma_f32_16x16x128_f8f6f4 v[68:71], v[160:167], v[198:205], v[68:71]
	s_setprio 0
	s_barrier
	s_add_u32 s80, s52, 0x40000
	s_addc_u32 s81, s53, 0
	s_add_i32 s75, s75, s55
	v_lshl_add_u64 v[176:177], s[80:81], 0, v[136:137]
	s_mov_b32 m0, s75
	ds_read_b128 v[168:171], v150 offset:16384
	ds_read_b128 v[182:185], v150 offset:18432
	ds_read_b128 v[172:175], v151 offset:16384
	ds_read_b128 v[186:189], v151 offset:18432
	ds_read_b128 v[190:193], v150 offset:20480
	ds_read_b128 v[198:201], v150 offset:22528
	ds_read_b128 v[194:197], v151 offset:20480
	ds_read_b128 v[202:205], v151 offset:22528
	global_load_lds_dwordx4 v[176:177], off
	v_lshl_add_u64 v[176:177], s[80:81], 0, v[132:133]
	s_add_i32 m0, s75, 0x2000
	s_nop 0
	global_load_lds_dwordx4 v[176:177], off
	s_waitcnt vmcnt(6)
	s_waitcnt lgkmcnt(0)
	s_barrier
	s_setprio 1
	s_waitcnt lgkmcnt(0)
	v_mfma_f32_16x16x128_f8f6f4 v[52:55], v[152:159], v[168:175], v[52:55]
	v_mfma_f32_16x16x128_f8f6f4 v[44:47], v[160:167], v[168:175], v[44:47]
	v_mfma_f32_16x16x128_f8f6f4 v[36:39], v[152:159], v[182:189], v[36:39]
	v_mfma_f32_16x16x128_f8f6f4 v[28:31], v[160:167], v[182:189], v[28:31]
	v_mfma_f32_16x16x128_f8f6f4 v[20:23], v[152:159], v[190:197], v[20:23]
	v_mfma_f32_16x16x128_f8f6f4 v[12:15], v[160:167], v[190:197], v[12:15]
	v_mfma_f32_16x16x128_f8f6f4 v[8:11], v[152:159], v[198:205], v[8:11]
	v_mfma_f32_16x16x128_f8f6f4 v[4:7], v[160:167], v[198:205], v[4:7]
	s_setprio 0
	s_barrier
	s_add_u32 s80, s50, 0x40000
	s_addc_u32 s81, s51, 0
	s_mov_b32 m0, s58
	v_lshl_add_u64 v[176:177], s[80:81], 0, v[2:3]
	global_load_lds_dwordx4 v[176:177], off
	v_lshl_add_u64 v[176:177], s[80:81], 0, v[134:135]
	s_mov_b32 m0, s59
	s_nop 0
	global_load_lds_dwordx4 v[176:177], off
	s_waitcnt vmcnt(6)
	s_waitcnt lgkmcnt(0)
	s_barrier
	s_setprio 1
	s_waitcnt lgkmcnt(0)
	v_mfma_f32_16x16x128_f8f6f4 v[64:67], v[222:229], v[168:175], v[64:67]
	v_mfma_f32_16x16x128_f8f6f4 v[60:63], v[230:237], v[168:175], v[60:63]
	v_mfma_f32_16x16x128_f8f6f4 v[56:59], v[222:229], v[182:189], v[56:59]
	v_mfma_f32_16x16x128_f8f6f4 v[48:51], v[230:237], v[182:189], v[48:51]
	v_mfma_f32_16x16x128_f8f6f4 v[40:43], v[222:229], v[190:197], v[40:43]
	v_mfma_f32_16x16x128_f8f6f4 v[32:35], v[230:237], v[190:197], v[32:35]
	v_mfma_f32_16x16x128_f8f6f4 v[24:27], v[222:229], v[198:205], v[24:27]
	v_mfma_f32_16x16x128_f8f6f4 v[16:19], v[230:237], v[198:205], v[16:19]
	s_setprio 0
	s_barrier
	v_add_u32_e32 v220, s31, v147
	v_add_u32_e32 v221, s31, v148
	ds_read_b128 v[222:225], v220
	ds_read_b128 v[230:233], v220 offset:2048
	ds_read_b128 v[226:229], v221
	ds_read_b128 v[234:237], v221 offset:2048
	s_add_i32 s74, s74, s55
	v_lshl_add_u64 v[176:177], s[52:53], 0, v[136:137]
	s_mov_b32 m0, s74
	ds_read_b128 v[168:171], v150 offset:32768
	ds_read_b128 v[182:185], v150 offset:34816
	ds_read_b128 v[172:175], v151 offset:32768
	ds_read_b128 v[186:189], v151 offset:34816
	ds_read_b128 v[190:193], v150 offset:36864
	ds_read_b128 v[198:201], v150 offset:38912
	ds_read_b128 v[194:197], v151 offset:36864
	ds_read_b128 v[202:205], v151 offset:38912
	global_load_lds_dwordx4 v[176:177], off
	v_lshl_add_u64 v[176:177], s[52:53], 0, v[132:133]
	s_add_i32 m0, s74, 0x2000
	s_nop 0
	global_load_lds_dwordx4 v[176:177], off
	s_waitcnt vmcnt(6)
	s_waitcnt lgkmcnt(0)
	s_barrier
	s_setprio 1
	s_waitcnt lgkmcnt(0)
	v_mfma_f32_16x16x128_f8f6f4 v[128:131], v[222:229], v[168:175], v[128:131]
	v_mfma_f32_16x16x128_f8f6f4 v[124:127], v[230:237], v[168:175], v[124:127]
	v_mfma_f32_16x16x128_f8f6f4 v[120:123], v[222:229], v[182:189], v[120:123]
	v_mfma_f32_16x16x128_f8f6f4 v[112:115], v[230:237], v[182:189], v[112:115]
	v_mfma_f32_16x16x128_f8f6f4 v[104:107], v[222:229], v[190:197], v[104:107]
	v_mfma_f32_16x16x128_f8f6f4 v[96:99], v[230:237], v[190:197], v[96:99]
	v_mfma_f32_16x16x128_f8f6f4 v[88:91], v[222:229], v[198:205], v[88:91]
	v_mfma_f32_16x16x128_f8f6f4 v[80:83], v[230:237], v[198:205], v[80:83]
	s_setprio 0
	s_barrier
	s_add_i32 s74, 0, 0x1c000
	s_mov_b32 m0, s60
	v_add_u32_e32 v156, s74, v147
	v_add_u32_e32 v164, s74, v148
	v_lshl_add_u64 v[142:143], v[142:143], 0, s[20:21]
	ds_read_b128 v[152:155], v156
	ds_read_b128 v[160:163], v156 offset:2048
	ds_read_b128 v[156:159], v164
	ds_read_b128 v[164:167], v164 offset:2048
	global_load_lds_dwordx4 v[142:143], off
	v_lshl_add_u64 v[142:143], v[144:145], 0, s[20:21]
	s_mov_b32 m0, s61
	s_nop 0
	global_load_lds_dwordx4 v[142:143], off
	s_waitcnt vmcnt(6)
	s_waitcnt lgkmcnt(0)
	s_barrier
	s_setprio 1
	s_waitcnt lgkmcnt(0)
	v_mfma_f32_16x16x128_f8f6f4 v[116:119], v[152:159], v[168:175], v[116:119]
	v_mfma_f32_16x16x128_f8f6f4 v[108:111], v[160:167], v[168:175], v[108:111]
	v_mfma_f32_16x16x128_f8f6f4 v[100:103], v[152:159], v[182:189], v[100:103]
	v_mfma_f32_16x16x128_f8f6f4 v[92:95], v[160:167], v[182:189], v[92:95]
	v_mfma_f32_16x16x128_f8f6f4 v[84:87], v[152:159], v[190:197], v[84:87]
	v_mfma_f32_16x16x128_f8f6f4 v[76:79], v[160:167], v[190:197], v[76:79]
	v_mfma_f32_16x16x128_f8f6f4 v[72:75], v[152:159], v[198:205], v[72:75]
	v_mfma_f32_16x16x128_f8f6f4 v[68:71], v[160:167], v[198:205], v[68:71]
	s_setprio 0
	s_barrier
	s_add_u32 s52, s52, 0x40080
	s_addc_u32 s53, s53, 0
	s_add_i32 s74, s74, s55
	v_lshl_add_u64 v[142:143], s[52:53], 0, v[136:137]
	s_mov_b32 m0, s74
	ds_read_b128 v[168:171], v150 offset:49152
	ds_read_b128 v[182:185], v150 offset:51200
	ds_read_b128 v[172:175], v151 offset:49152
	ds_read_b128 v[186:189], v151 offset:51200
	ds_read_b128 v[190:193], v150 offset:53248
	ds_read_b128 v[198:201], v150 offset:55296
	ds_read_b128 v[194:197], v151 offset:53248
	ds_read_b128 v[202:205], v151 offset:55296
	global_load_lds_dwordx4 v[142:143], off
	v_lshl_add_u64 v[142:143], s[52:53], 0, v[132:133]
	s_add_i32 m0, s74, 0x2000
	s_nop 0
	global_load_lds_dwordx4 v[142:143], off
	s_waitcnt vmcnt(6)
	s_waitcnt lgkmcnt(0)
	s_barrier
	s_setprio 1
	s_waitcnt lgkmcnt(0)
	v_mfma_f32_16x16x128_f8f6f4 v[52:55], v[152:159], v[168:175], v[52:55]
	v_mfma_f32_16x16x128_f8f6f4 v[44:47], v[160:167], v[168:175], v[44:47]
	v_mfma_f32_16x16x128_f8f6f4 v[36:39], v[152:159], v[182:189], v[36:39]
	v_mfma_f32_16x16x128_f8f6f4 v[28:31], v[160:167], v[182:189], v[28:31]
	v_mfma_f32_16x16x128_f8f6f4 v[20:23], v[152:159], v[190:197], v[20:23]
	v_mfma_f32_16x16x128_f8f6f4 v[12:15], v[160:167], v[190:197], v[12:15]
	v_mfma_f32_16x16x128_f8f6f4 v[8:11], v[152:159], v[198:205], v[8:11]
	v_mfma_f32_16x16x128_f8f6f4 v[4:7], v[160:167], v[198:205], v[4:7]
	s_setprio 0
	s_barrier
	s_add_u32 s50, s50, 0x40080
	s_addc_u32 s51, s51, 0
	s_mov_b32 m0, s62
	v_lshl_add_u64 v[142:143], s[50:51], 0, v[2:3]
	global_load_lds_dwordx4 v[142:143], off
	v_lshl_add_u64 v[142:143], s[50:51], 0, v[134:135]
	s_mov_b32 m0, s63
	s_nop 0
	global_load_lds_dwordx4 v[142:143], off
	s_waitcnt vmcnt(6)
	s_waitcnt lgkmcnt(0)
	s_barrier
	s_setprio 1
	s_waitcnt lgkmcnt(0)
	v_mfma_f32_16x16x128_f8f6f4 v[64:67], v[222:229], v[168:175], v[64:67]
	v_mfma_f32_16x16x128_f8f6f4 v[60:63], v[230:237], v[168:175], v[60:63]
	v_mfma_f32_16x16x128_f8f6f4 v[56:59], v[222:229], v[182:189], v[56:59]
	v_mfma_f32_16x16x128_f8f6f4 v[48:51], v[230:237], v[182:189], v[48:51]
	v_mfma_f32_16x16x128_f8f6f4 v[40:43], v[222:229], v[190:197], v[40:43]
	v_mfma_f32_16x16x128_f8f6f4 v[32:35], v[230:237], v[190:197], v[32:35]
	v_mfma_f32_16x16x128_f8f6f4 v[24:27], v[222:229], v[198:205], v[24:27]
	v_mfma_f32_16x16x128_f8f6f4 v[16:19], v[230:237], v[198:205], v[16:19]
	s_setprio 0
	s_barrier
	s_add_i32 s73, s73, 2
	s_add_u32 s67, s67, 0x100
	s_addc_u32 s72, s72, 0
	s_add_u32 s48, s48, 0x100
	s_addc_u32 s49, s49, 0
	s_cmp_gt_u32 s73, 13
	s_cbranch_scc0 .LBB0_247
	v_lshl_or_b32 v144, s65, 8, v149
	v_lshl_add_u32 v156, s66, 8, v146
	v_ashrrev_i32_e32 v145, 31, v144
	v_mov_b64_e32 v[142:143], s[0:1]
	v_mad_i64_i32 v[152:153], s[8:9], v156, s94, v[142:143]
	v_lshlrev_b64 v[144:145], 1, v[144:145]
	v_pk_mul_f32 v[130:131], v[130:131], s[22:23] op_sel_hi:[1,0]
	v_pk_mul_f32 v[128:129], v[128:129], s[22:23] op_sel_hi:[1,0]
	v_pk_mul_f32 v[154:155], v[126:127], s[22:23] op_sel_hi:[1,0]
	v_pk_mul_f32 v[126:127], v[124:125], s[22:23] op_sel_hi:[1,0]
	v_lshl_add_u64 v[152:153], v[152:153], 0, v[144:145]
	v_cvt_pk_bf16_f32 v124, v128, v129
	v_cvt_pk_bf16_f32 v125, v130, v131
	v_cvt_pk_bf16_f32 v126, v126, v127
	v_cvt_pk_bf16_f32 v127, v154, v155
	global_store_dwordx4 v[152:153], v[124:127], off
	v_pk_mul_f32 v[118:119], v[118:119], s[22:23] op_sel_hi:[1,0]
	v_pk_mul_f32 v[116:117], v[116:117], s[22:23] op_sel_hi:[1,0]
	v_pk_mul_f32 v[124:125], v[110:111], s[22:23] op_sel_hi:[1,0]
	v_pk_mul_f32 v[110:111], v[108:109], s[22:23] op_sel_hi:[1,0]
	v_cvt_pk_bf16_f32 v108, v116, v117
	v_cvt_pk_bf16_f32 v109, v118, v119
	v_cvt_pk_bf16_f32 v110, v110, v111
	v_cvt_pk_bf16_f32 v111, v124, v125
	global_store_dwordx4 v[152:153], v[108:111], off offset:256
	v_pk_mul_f32 v[114:115], v[114:115], s[22:23] op_sel_hi:[1,0]
	v_pk_mul_f32 v[112:113], v[112:113], s[22:23] op_sel_hi:[1,0]
	v_or_b32_e32 v108, 16, v156
	v_mad_i64_i32 v[108:109], s[8:9], v108, s94, v[142:143]
	v_lshl_add_u64 v[116:117], v[108:109], 0, v[144:145]
	v_pk_mul_f32 v[110:111], v[122:123], s[22:23] op_sel_hi:[1,0]
	v_pk_mul_f32 v[108:109], v[120:121], s[22:23] op_sel_hi:[1,0]
	v_pk_mul_f32 v[102:103], v[102:103], s[22:23] op_sel_hi:[1,0]
	v_cvt_pk_bf16_f32 v108, v108, v109
	v_cvt_pk_bf16_f32 v109, v110, v111
	v_cvt_pk_bf16_f32 v110, v112, v113
	v_cvt_pk_bf16_f32 v111, v114, v115
	global_store_dwordx4 v[116:117], v[108:111], off
	v_pk_mul_f32 v[100:101], v[100:101], s[22:23] op_sel_hi:[1,0]
	v_pk_mul_f32 v[98:99], v[98:99], s[22:23] op_sel_hi:[1,0]
	v_pk_mul_f32 v[108:109], v[94:95], s[22:23] op_sel_hi:[1,0]
	v_pk_mul_f32 v[94:95], v[92:93], s[22:23] op_sel_hi:[1,0]
	v_cvt_pk_bf16_f32 v92, v100, v101
	v_cvt_pk_bf16_f32 v93, v102, v103
	v_cvt_pk_bf16_f32 v94, v94, v95
	v_cvt_pk_bf16_f32 v95, v108, v109
	global_store_dwordx4 v[116:117], v[92:95], off offset:256
	v_pk_mul_f32 v[96:97], v[96:97], s[22:23] op_sel_hi:[1,0]
	v_pk_mul_f32 v[86:87], v[86:87], s[22:23] op_sel_hi:[1,0]
	v_or_b32_e32 v92, 32, v156
	v_mad_i64_i32 v[92:93], s[8:9], v92, s94, v[142:143]
	v_lshl_add_u64 v[100:101], v[92:93], 0, v[144:145]
	v_pk_mul_f32 v[94:95], v[106:107], s[22:23] op_sel_hi:[1,0]
	v_pk_mul_f32 v[92:93], v[104:105], s[22:23] op_sel_hi:[1,0]
	v_pk_mul_f32 v[84:85], v[84:85], s[22:23] op_sel_hi:[1,0]
	v_cvt_pk_bf16_f32 v92, v92, v93
	v_cvt_pk_bf16_f32 v93, v94, v95
	v_cvt_pk_bf16_f32 v94, v96, v97
	v_cvt_pk_bf16_f32 v95, v98, v99
	global_store_dwordx4 v[100:101], v[92:95], off
	v_pk_mul_f32 v[82:83], v[82:83], s[22:23] op_sel_hi:[1,0]
	v_pk_mul_f32 v[80:81], v[80:81], s[22:23] op_sel_hi:[1,0]
	v_pk_mul_f32 v[92:93], v[78:79], s[22:23] op_sel_hi:[1,0]
	v_pk_mul_f32 v[78:79], v[76:77], s[22:23] op_sel_hi:[1,0]
	v_cvt_pk_bf16_f32 v76, v84, v85
	v_cvt_pk_bf16_f32 v77, v86, v87
	v_cvt_pk_bf16_f32 v78, v78, v79
	v_cvt_pk_bf16_f32 v79, v92, v93
	global_store_dwordx4 v[100:101], v[76:79], off offset:256
	v_pk_mul_f32 v[74:75], v[74:75], s[22:23] op_sel_hi:[1,0]
	v_pk_mul_f32 v[72:73], v[72:73], s[22:23] op_sel_hi:[1,0]
	v_or_b32_e32 v76, 48, v156
	v_mad_i64_i32 v[76:77], s[8:9], v76, s94, v[142:143]
	v_lshl_add_u64 v[84:85], v[76:77], 0, v[144:145]
	v_pk_mul_f32 v[78:79], v[90:91], s[22:23] op_sel_hi:[1,0]
	v_pk_mul_f32 v[76:77], v[88:89], s[22:23] op_sel_hi:[1,0]
	v_pk_mul_f32 v[66:67], v[66:67], s[22:23] op_sel_hi:[1,0]
	v_cvt_pk_bf16_f32 v76, v76, v77
	v_cvt_pk_bf16_f32 v77, v78, v79
	v_cvt_pk_bf16_f32 v78, v80, v81
	v_cvt_pk_bf16_f32 v79, v82, v83
	global_store_dwordx4 v[84:85], v[76:79], off
	v_pk_mul_f32 v[64:65], v[64:65], s[22:23] op_sel_hi:[1,0]
	v_pk_mul_f32 v[54:55], v[54:55], s[22:23] op_sel_hi:[1,0]
	v_pk_mul_f32 v[76:77], v[70:71], s[22:23] op_sel_hi:[1,0]
	v_pk_mul_f32 v[70:71], v[68:69], s[22:23] op_sel_hi:[1,0]
	v_cvt_pk_bf16_f32 v68, v72, v73
	v_cvt_pk_bf16_f32 v69, v74, v75
	v_cvt_pk_bf16_f32 v70, v70, v71
	v_cvt_pk_bf16_f32 v71, v76, v77
	global_store_dwordx4 v[84:85], v[68:71], off offset:256
	v_pk_mul_f32 v[52:53], v[52:53], s[22:23] op_sel_hi:[1,0]
	v_pk_mul_f32 v[50:51], v[50:51], s[22:23] op_sel_hi:[1,0]
	v_add_u32_e32 v68, 0x80, v156
	v_mad_i64_i32 v[68:69], s[8:9], v68, s94, v[142:143]
	v_pk_mul_f32 v[70:71], v[62:63], s[22:23] op_sel_hi:[1,0]
	v_pk_mul_f32 v[62:63], v[60:61], s[22:23] op_sel_hi:[1,0]
	v_lshl_add_u64 v[68:69], v[68:69], 0, v[144:145]
	v_cvt_pk_bf16_f32 v60, v64, v65
	v_cvt_pk_bf16_f32 v61, v66, v67
	v_cvt_pk_bf16_f32 v62, v62, v63
	v_cvt_pk_bf16_f32 v63, v70, v71
	global_store_dwordx4 v[68:69], v[60:63], off
	v_pk_mul_f32 v[48:49], v[48:49], s[22:23] op_sel_hi:[1,0]
	v_pk_mul_f32 v[38:39], v[38:39], s[22:23] op_sel_hi:[1,0]
	v_pk_mul_f32 v[60:61], v[46:47], s[22:23] op_sel_hi:[1,0]
	v_pk_mul_f32 v[46:47], v[44:45], s[22:23] op_sel_hi:[1,0]
	v_cvt_pk_bf16_f32 v44, v52, v53
	v_cvt_pk_bf16_f32 v45, v54, v55
	v_cvt_pk_bf16_f32 v46, v46, v47
	v_cvt_pk_bf16_f32 v47, v60, v61
	global_store_dwordx4 v[68:69], v[44:47], off offset:256
	v_pk_mul_f32 v[36:37], v[36:37], s[22:23] op_sel_hi:[1,0]
	v_pk_mul_f32 v[34:35], v[34:35], s[22:23] op_sel_hi:[1,0]
	v_add_u32_e32 v44, 0x90, v156
	v_mad_i64_i32 v[44:45], s[8:9], v44, s94, v[142:143]
	v_lshl_add_u64 v[52:53], v[44:45], 0, v[144:145]
	v_pk_mul_f32 v[46:47], v[58:59], s[22:23] op_sel_hi:[1,0]
	v_pk_mul_f32 v[44:45], v[56:57], s[22:23] op_sel_hi:[1,0]
	v_pk_mul_f32 v[32:33], v[32:33], s[22:23] op_sel_hi:[1,0]
	v_cvt_pk_bf16_f32 v44, v44, v45
	v_cvt_pk_bf16_f32 v45, v46, v47
	v_cvt_pk_bf16_f32 v46, v48, v49
	v_cvt_pk_bf16_f32 v47, v50, v51
	global_store_dwordx4 v[52:53], v[44:47], off
	v_pk_mul_f32 v[22:23], v[22:23], s[22:23] op_sel_hi:[1,0]
	v_pk_mul_f32 v[20:21], v[20:21], s[22:23] op_sel_hi:[1,0]
	v_pk_mul_f32 v[44:45], v[30:31], s[22:23] op_sel_hi:[1,0]
	v_pk_mul_f32 v[30:31], v[28:29], s[22:23] op_sel_hi:[1,0]
	v_cvt_pk_bf16_f32 v28, v36, v37
	v_cvt_pk_bf16_f32 v29, v38, v39
	v_cvt_pk_bf16_f32 v30, v30, v31
	v_cvt_pk_bf16_f32 v31, v44, v45
	global_store_dwordx4 v[52:53], v[28:31], off offset:256
	v_pk_mul_f32 v[18:19], v[18:19], s[22:23] op_sel_hi:[1,0]
	v_pk_mul_f32 v[16:17], v[16:17], s[22:23] op_sel_hi:[1,0]
	v_add_u32_e32 v28, 0xa0, v156
	v_mad_i64_i32 v[28:29], s[8:9], v28, s94, v[142:143]
	v_lshl_add_u64 v[36:37], v[28:29], 0, v[144:145]
	v_pk_mul_f32 v[30:31], v[42:43], s[22:23] op_sel_hi:[1,0]
	v_pk_mul_f32 v[28:29], v[40:41], s[22:23] op_sel_hi:[1,0]
	v_pk_mul_f32 v[10:11], v[10:11], s[22:23] op_sel_hi:[1,0]
	v_cvt_pk_bf16_f32 v28, v28, v29
	v_cvt_pk_bf16_f32 v29, v30, v31
	v_cvt_pk_bf16_f32 v30, v32, v33
	v_cvt_pk_bf16_f32 v31, v34, v35
	global_store_dwordx4 v[36:37], v[28:31], off
	v_pk_mul_f32 v[8:9], v[8:9], s[22:23] op_sel_hi:[1,0]
	s_and_b64 vcc, exec, s[40:41]
	v_pk_mul_f32 v[28:29], v[14:15], s[22:23] op_sel_hi:[1,0]
	v_pk_mul_f32 v[14:15], v[12:13], s[22:23] op_sel_hi:[1,0]
	v_cvt_pk_bf16_f32 v12, v20, v21
	v_cvt_pk_bf16_f32 v13, v22, v23
	v_cvt_pk_bf16_f32 v14, v14, v15
	v_cvt_pk_bf16_f32 v15, v28, v29
	global_store_dwordx4 v[36:37], v[12:15], off offset:256
	s_mov_b32 s65, s4
	s_mov_b32 s66, s42
	v_add_u32_e32 v12, 0xb0, v156
	v_mad_i64_i32 v[12:13], s[8:9], v12, s94, v[142:143]
	v_lshl_add_u64 v[20:21], v[12:13], 0, v[144:145]
	v_pk_mul_f32 v[14:15], v[26:27], s[22:23] op_sel_hi:[1,0]
	v_pk_mul_f32 v[12:13], v[24:25], s[22:23] op_sel_hi:[1,0]
	s_mov_b64 s[48:49], s[46:47]
	v_cvt_pk_bf16_f32 v12, v12, v13
	v_cvt_pk_bf16_f32 v13, v14, v15
	v_cvt_pk_bf16_f32 v14, v16, v17
	v_cvt_pk_bf16_f32 v15, v18, v19
	global_store_dwordx4 v[20:21], v[12:15], off
	s_mov_b64 s[50:51], s[44:45]
	s_nop 0
	v_pk_mul_f32 v[12:13], v[6:7], s[22:23] op_sel_hi:[1,0]
	v_pk_mul_f32 v[6:7], v[4:5], s[22:23] op_sel_hi:[1,0]
	v_cvt_pk_bf16_f32 v4, v8, v9
	v_cvt_pk_bf16_f32 v5, v10, v11
	v_cvt_pk_bf16_f32 v6, v6, v7
	v_cvt_pk_bf16_f32 v7, v12, v13
	global_store_dwordx4 v[20:21], v[4:7], off offset:256
	s_cbranch_vccz .LBB0_240
	s_waitcnt vmcnt(0)
	v_readlane_b32 s64, v253, 27
	v_readlane_b32 s66, v253, 29
	s_cmpk_gt_u32 s6, 0xff
	v_readlane_b32 s65, v253, 28
	v_readlane_b32 s67, v253, 30
	s_cbranch_scc1 .LBB0_251
	s_barrier

.LBB0_430:
	s_add_u32 s56, s54, 0x80
	s_addc_u32 s57, s55, 0
	s_add_i32 vcc_lo, 0, 0x10000
	v_add_u32_e32 v220, vcc_lo, v143
	v_add_u32_e32 v221, vcc_lo, v144
	ds_read_b128 v[222:225], v220
	ds_read_b128 v[230:233], v220 offset:2048
	ds_read_b128 v[226:229], v221
	ds_read_b128 v[234:237], v221 offset:2048
	s_cmp_eq_u32 s97, 12
	s_cselect_b32 s59, s5, s57
	s_cselect_b32 s58, s43, s56
	s_cselect_b32 s57, s8, s96
	s_cselect_b32 s56, s9, s89
	s_add_i32 s76, s31, s64
	v_lshl_add_u64 v[172:173], s[54:55], 0, v[140:141]
	s_mov_b32 m0, s76
	ds_read_b128 v[164:167], v146
	ds_read_b128 v[182:185], v146 offset:2048
	ds_read_b128 v[168:171], v147
	ds_read_b128 v[186:189], v147 offset:2048
	ds_read_b128 v[190:193], v146 offset:4096
	ds_read_b128 v[198:201], v146 offset:6144
	ds_read_b128 v[194:197], v147 offset:4096
	ds_read_b128 v[202:205], v147 offset:6144
	global_load_lds_dwordx4 v[172:173], off
	v_lshl_add_u64 v[172:173], s[54:55], 0, v[138:139]
	s_add_i32 m0, s76, 0x2000
	s_nop 0
	global_load_lds_dwordx4 v[172:173], off
	s_waitcnt vmcnt(6)
	s_waitcnt lgkmcnt(0)
	s_barrier
	s_setprio 1
	s_waitcnt lgkmcnt(0)
	v_mfma_f32_16x16x128_f8f6f4 v[128:131], v[222:229], v[164:171], v[128:131]
	v_mfma_f32_16x16x128_f8f6f4 v[124:127], v[230:237], v[164:171], v[124:127]
	v_mfma_f32_16x16x128_f8f6f4 v[116:119], v[222:229], v[182:189], v[116:119]
	v_mfma_f32_16x16x128_f8f6f4 v[108:111], v[230:237], v[182:189], v[108:111]
	v_mfma_f32_16x16x128_f8f6f4 v[100:103], v[222:229], v[190:197], v[100:103]
	v_mfma_f32_16x16x128_f8f6f4 v[92:95], v[230:237], v[190:197], v[92:95]
	v_mfma_f32_16x16x128_f8f6f4 v[84:87], v[222:229], v[198:205], v[84:87]
	v_mfma_f32_16x16x128_f8f6f4 v[76:79], v[230:237], v[198:205], v[76:79]
	s_setprio 0
	s_barrier
	s_add_i32 s76, 0, 0x14000
	s_mov_b32 m0, s45
	v_add_u32_e32 v152, s76, v143
	v_add_u32_e32 v160, s76, v144
	v_lshl_add_u64 v[172:173], s[56:57], 0, v[2:3]
	ds_read_b128 v[148:151], v152
	ds_read_b128 v[156:159], v152 offset:2048
	ds_read_b128 v[152:155], v160
	ds_read_b128 v[160:163], v160 offset:2048
	global_load_lds_dwordx4 v[172:173], off
	v_lshl_add_u64 v[174:175], s[56:57], 0, v[134:135]
	s_mov_b32 m0, s51
	s_nop 0
	global_load_lds_dwordx4 v[174:175], off
	s_waitcnt vmcnt(6)
	s_waitcnt lgkmcnt(0)
	s_barrier
	s_setprio 1
	s_waitcnt lgkmcnt(0)
	v_mfma_f32_16x16x128_f8f6f4 v[120:123], v[148:155], v[164:171], v[120:123]
	v_mfma_f32_16x16x128_f8f6f4 v[112:115], v[156:163], v[164:171], v[112:115]
	v_mfma_f32_16x16x128_f8f6f4 v[104:107], v[148:155], v[182:189], v[104:107]
	v_mfma_f32_16x16x128_f8f6f4 v[96:99], v[156:163], v[182:189], v[96:99]
	v_mfma_f32_16x16x128_f8f6f4 v[88:91], v[148:155], v[190:197], v[88:91]
	v_mfma_f32_16x16x128_f8f6f4 v[80:83], v[156:163], v[190:197], v[80:83]
	v_mfma_f32_16x16x128_f8f6f4 v[72:75], v[148:155], v[198:205], v[72:75]
	v_mfma_f32_16x16x128_f8f6f4 v[68:71], v[156:163], v[198:205], v[68:71]
	s_setprio 0
	s_barrier
	s_add_u32 s80, s58, 0x40000
	s_addc_u32 s81, s59, 0
	s_add_i32 s76, s76, s64
	v_lshl_add_u64 v[176:177], s[80:81], 0, v[136:137]
	s_mov_b32 m0, s76
	ds_read_b128 v[164:167], v146 offset:16384
	ds_read_b128 v[182:185], v146 offset:18432
	ds_read_b128 v[168:171], v147 offset:16384
	ds_read_b128 v[186:189], v147 offset:18432
	ds_read_b128 v[190:193], v146 offset:20480
	ds_read_b128 v[198:201], v146 offset:22528
	ds_read_b128 v[194:197], v147 offset:20480
	ds_read_b128 v[202:205], v147 offset:22528
	global_load_lds_dwordx4 v[176:177], off
	v_lshl_add_u64 v[176:177], s[80:81], 0, v[132:133]
	s_add_i32 m0, s76, 0x2000
	s_nop 0
	global_load_lds_dwordx4 v[176:177], off
	s_waitcnt vmcnt(6)
	s_waitcnt lgkmcnt(0)
	s_barrier
	s_setprio 1
	s_waitcnt lgkmcnt(0)
	v_mfma_f32_16x16x128_f8f6f4 v[56:59], v[148:155], v[164:171], v[56:59]
	v_mfma_f32_16x16x128_f8f6f4 v[48:51], v[156:163], v[164:171], v[48:51]
	v_mfma_f32_16x16x128_f8f6f4 v[40:43], v[148:155], v[182:189], v[40:43]
	v_mfma_f32_16x16x128_f8f6f4 v[32:35], v[156:163], v[182:189], v[32:35]
	v_mfma_f32_16x16x128_f8f6f4 v[24:27], v[148:155], v[190:197], v[24:27]
	v_mfma_f32_16x16x128_f8f6f4 v[16:19], v[156:163], v[190:197], v[16:19]
	v_mfma_f32_16x16x128_f8f6f4 v[8:11], v[148:155], v[198:205], v[8:11]
	v_mfma_f32_16x16x128_f8f6f4 v[4:7], v[156:163], v[198:205], v[4:7]
	s_setprio 0
	s_barrier
	s_add_u32 s80, s56, 0x40000
	s_addc_u32 s81, s57, 0
	s_mov_b32 m0, s66
	v_lshl_add_u64 v[176:177], s[80:81], 0, v[2:3]
	global_load_lds_dwordx4 v[176:177], off
	v_lshl_add_u64 v[176:177], s[80:81], 0, v[134:135]
	s_mov_b32 m0, s67
	s_nop 0
	global_load_lds_dwordx4 v[176:177], off
	s_waitcnt vmcnt(6)
	s_waitcnt lgkmcnt(0)
	s_barrier
	s_setprio 1
	s_waitcnt lgkmcnt(0)
	v_mfma_f32_16x16x128_f8f6f4 v[64:67], v[222:229], v[164:171], v[64:67]
	v_mfma_f32_16x16x128_f8f6f4 v[60:63], v[230:237], v[164:171], v[60:63]
	v_mfma_f32_16x16x128_f8f6f4 v[52:55], v[222:229], v[182:189], v[52:55]
	v_mfma_f32_16x16x128_f8f6f4 v[44:47], v[230:237], v[182:189], v[44:47]
	v_mfma_f32_16x16x128_f8f6f4 v[36:39], v[222:229], v[190:197], v[36:39]
	v_mfma_f32_16x16x128_f8f6f4 v[28:31], v[230:237], v[190:197], v[28:31]
	v_mfma_f32_16x16x128_f8f6f4 v[20:23], v[222:229], v[198:205], v[20:23]
	v_mfma_f32_16x16x128_f8f6f4 v[12:15], v[230:237], v[198:205], v[12:15]
	s_setprio 0
	s_barrier
	v_add_u32_e32 v220, s31, v143
	v_add_u32_e32 v221, s31, v144
	ds_read_b128 v[222:225], v220
	ds_read_b128 v[230:233], v220 offset:2048
	ds_read_b128 v[226:229], v221
	ds_read_b128 v[234:237], v221 offset:2048
	s_add_i32 s76, vcc_lo, s64
	v_lshl_add_u64 v[176:177], s[58:59], 0, v[136:137]
	s_mov_b32 m0, s76
	ds_read_b128 v[164:167], v146 offset:32768
	ds_read_b128 v[182:185], v146 offset:34816
	ds_read_b128 v[168:171], v147 offset:32768
	ds_read_b128 v[186:189], v147 offset:34816
	ds_read_b128 v[190:193], v146 offset:36864
	ds_read_b128 v[198:201], v146 offset:38912
	ds_read_b128 v[194:197], v147 offset:36864
	ds_read_b128 v[202:205], v147 offset:38912
	global_load_lds_dwordx4 v[176:177], off
	v_lshl_add_u64 v[176:177], s[58:59], 0, v[132:133]
	s_add_i32 m0, s76, 0x2000
	s_nop 0
	global_load_lds_dwordx4 v[176:177], off
	s_waitcnt vmcnt(6)
	s_waitcnt lgkmcnt(0)
	s_barrier
	s_setprio 1
	s_waitcnt lgkmcnt(0)
	v_mfma_f32_16x16x128_f8f6f4 v[128:131], v[222:229], v[164:171], v[128:131]
	v_mfma_f32_16x16x128_f8f6f4 v[124:127], v[230:237], v[164:171], v[124:127]
	v_mfma_f32_16x16x128_f8f6f4 v[116:119], v[222:229], v[182:189], v[116:119]
	v_mfma_f32_16x16x128_f8f6f4 v[108:111], v[230:237], v[182:189], v[108:111]
	v_mfma_f32_16x16x128_f8f6f4 v[100:103], v[222:229], v[190:197], v[100:103]
	v_mfma_f32_16x16x128_f8f6f4 v[92:95], v[230:237], v[190:197], v[92:95]
	v_mfma_f32_16x16x128_f8f6f4 v[84:87], v[222:229], v[198:205], v[84:87]
	v_mfma_f32_16x16x128_f8f6f4 v[76:79], v[230:237], v[198:205], v[76:79]
	s_setprio 0
	s_barrier
	s_add_i32 s76, 0, 0x1c000
	s_mov_b32 m0, s72
	v_add_u32_e32 v152, s76, v143
	v_add_u32_e32 v160, s76, v144
	v_lshl_add_u64 v[172:173], v[172:173], 0, s[20:21]
	ds_read_b128 v[148:151], v152
	ds_read_b128 v[156:159], v152 offset:2048
	ds_read_b128 v[152:155], v160
	ds_read_b128 v[160:163], v160 offset:2048
	global_load_lds_dwordx4 v[172:173], off
	v_lshl_add_u64 v[172:173], v[174:175], 0, s[20:21]
	s_mov_b32 m0, s73
	s_nop 0
	global_load_lds_dwordx4 v[172:173], off
	s_waitcnt vmcnt(6)
	s_waitcnt lgkmcnt(0)
	s_barrier
	s_setprio 1
	s_waitcnt lgkmcnt(0)
	v_mfma_f32_16x16x128_f8f6f4 v[120:123], v[148:155], v[164:171], v[120:123]
	v_mfma_f32_16x16x128_f8f6f4 v[112:115], v[156:163], v[164:171], v[112:115]
	v_mfma_f32_16x16x128_f8f6f4 v[104:107], v[148:155], v[182:189], v[104:107]
	v_mfma_f32_16x16x128_f8f6f4 v[96:99], v[156:163], v[182:189], v[96:99]
	v_mfma_f32_16x16x128_f8f6f4 v[88:91], v[148:155], v[190:197], v[88:91]
	v_mfma_f32_16x16x128_f8f6f4 v[80:83], v[156:163], v[190:197], v[80:83]
	v_mfma_f32_16x16x128_f8f6f4 v[72:75], v[148:155], v[198:205], v[72:75]
	v_mfma_f32_16x16x128_f8f6f4 v[68:71], v[156:163], v[198:205], v[68:71]
	s_setprio 0
	s_barrier
	s_add_u32 s58, s58, 0x40080
	s_addc_u32 s59, s59, 0
	s_add_i32 s76, s76, s64
	v_lshl_add_u64 v[172:173], s[58:59], 0, v[136:137]
	s_mov_b32 m0, s76
	ds_read_b128 v[164:167], v146 offset:49152
	ds_read_b128 v[182:185], v146 offset:51200
	ds_read_b128 v[168:171], v147 offset:49152
	ds_read_b128 v[186:189], v147 offset:51200
	ds_read_b128 v[190:193], v146 offset:53248
	ds_read_b128 v[198:201], v146 offset:55296
	ds_read_b128 v[194:197], v147 offset:53248
	ds_read_b128 v[202:205], v147 offset:55296
	global_load_lds_dwordx4 v[172:173], off
	v_lshl_add_u64 v[172:173], s[58:59], 0, v[132:133]
	s_add_i32 m0, s76, 0x2000
	s_nop 0
	global_load_lds_dwordx4 v[172:173], off
	s_waitcnt vmcnt(6)
	s_waitcnt lgkmcnt(0)
	s_barrier
	s_setprio 1
	s_waitcnt lgkmcnt(0)
	v_mfma_f32_16x16x128_f8f6f4 v[56:59], v[148:155], v[164:171], v[56:59]
	v_mfma_f32_16x16x128_f8f6f4 v[48:51], v[156:163], v[164:171], v[48:51]
	v_mfma_f32_16x16x128_f8f6f4 v[40:43], v[148:155], v[182:189], v[40:43]
	v_mfma_f32_16x16x128_f8f6f4 v[32:35], v[156:163], v[182:189], v[32:35]
	v_mfma_f32_16x16x128_f8f6f4 v[24:27], v[148:155], v[190:197], v[24:27]
	v_mfma_f32_16x16x128_f8f6f4 v[16:19], v[156:163], v[190:197], v[16:19]
	v_mfma_f32_16x16x128_f8f6f4 v[8:11], v[148:155], v[198:205], v[8:11]
	v_mfma_f32_16x16x128_f8f6f4 v[4:7], v[156:163], v[198:205], v[4:7]
	s_setprio 0
	s_barrier
	s_add_u32 s56, s56, 0x40080
	s_addc_u32 s57, s57, 0
	s_mov_b32 m0, s74
	v_lshl_add_u64 v[172:173], s[56:57], 0, v[2:3]
	global_load_lds_dwordx4 v[172:173], off
	v_lshl_add_u64 v[172:173], s[56:57], 0, v[134:135]
	s_mov_b32 m0, s75
	s_nop 0
	global_load_lds_dwordx4 v[172:173], off
	s_waitcnt vmcnt(6)
	s_waitcnt lgkmcnt(0)
	s_barrier
	s_setprio 1
	s_waitcnt lgkmcnt(0)
	v_mfma_f32_16x16x128_f8f6f4 v[64:67], v[222:229], v[164:171], v[64:67]
	v_mfma_f32_16x16x128_f8f6f4 v[60:63], v[230:237], v[164:171], v[60:63]
	v_mfma_f32_16x16x128_f8f6f4 v[52:55], v[222:229], v[182:189], v[52:55]
	v_mfma_f32_16x16x128_f8f6f4 v[44:47], v[230:237], v[182:189], v[44:47]
	v_mfma_f32_16x16x128_f8f6f4 v[36:39], v[222:229], v[190:197], v[36:39]
	v_mfma_f32_16x16x128_f8f6f4 v[28:31], v[230:237], v[190:197], v[28:31]
	v_mfma_f32_16x16x128_f8f6f4 v[20:23], v[222:229], v[198:205], v[20:23]
	v_mfma_f32_16x16x128_f8f6f4 v[12:15], v[230:237], v[198:205], v[12:15]
	s_setprio 0
	s_barrier
	s_add_i32 s97, s97, 2
	s_add_u32 s89, s89, 0x100
	s_addc_u32 s96, s96, 0
	s_add_u32 s54, s54, 0x100
	s_addc_u32 s55, s55, 0
	s_cmp_gt_u32 s97, 13
	s_cbranch_scc0 .LBB0_430
	v_mul_f32_e32 v152, 0x3c000000, v128
	v_mul_f32_e32 v129, 0x3c000000, v129
	v_mov_b32_e32 v128, v3
	v_cvt_pk_fp8_f32 v128, v152, v129
	v_mul_f32_e32 v124, 0x3c000000, v124
	v_mul_f32_e32 v125, 0x3c000000, v125
	v_mov_b32_e32 v129, v3
	v_cvt_pk_fp8_f32 v129, v124, v125
	v_mul_f32_e32 v124, 0x3c000000, v126
	v_mul_f32_e32 v125, 0x3c000000, v127
	v_mul_f32_e32 v121, 0x3c000000, v121
	v_cvt_pk_fp8_f32 v129, v124, v125 op_sel:[0,0,1]
	v_mul_f32_e32 v124, 0x3c000000, v120
	v_mov_b32_e32 v120, v3
	v_cvt_pk_fp8_f32 v120, v124, v121
	v_mul_f32_e32 v112, 0x3c000000, v112
	v_mul_f32_e32 v113, 0x3c000000, v113
	v_mov_b32_e32 v121, v3
	v_cvt_pk_fp8_f32 v121, v112, v113
	v_mul_f32_e32 v130, 0x3c000000, v130
	v_mul_f32_e32 v131, 0x3c000000, v131
	v_lshl_add_u32 v148, s50, 8, v142
	v_lshl_or_b32 v150, s44, 8, v145
	v_cvt_pk_fp8_f32 v128, v130, v131 op_sel:[0,0,1]
	v_mul_f32_e32 v122, 0x3c000000, v122
	v_mul_f32_e32 v123, 0x3c000000, v123
	v_mul_f32_e32 v112, 0x3c000000, v114
	v_mul_f32_e32 v113, 0x3c000000, v115
	v_ashrrev_i32_e32 v151, 31, v150
	v_ashrrev_i32_e32 v149, 31, v148
	v_cvt_pk_fp8_f32 v120, v122, v123 op_sel:[0,0,1]
	v_cvt_pk_fp8_f32 v121, v112, v113 op_sel:[0,0,1]
	v_lshl_add_u64 v[150:151], s[0:1], 0, v[150:151]
	v_lshlrev_b64 v[112:113], 11, v[148:149]
	v_lshl_add_u64 v[112:113], v[150:151], 0, v[112:113]
	global_store_dwordx2 v[112:113], v[128:129], off
	global_store_dwordx2 v[112:113], v[120:121], off offset:128
	v_mul_f32_e32 v120, 0x3c000000, v116
	v_mul_f32_e32 v117, 0x3c000000, v117
	v_mov_b32_e32 v116, v3
	v_cvt_pk_fp8_f32 v116, v120, v117
	v_mul_f32_e32 v108, 0x3c000000, v108
	v_mul_f32_e32 v109, 0x3c000000, v109
	v_mov_b32_e32 v117, v3
	v_cvt_pk_fp8_f32 v117, v108, v109
	v_mul_f32_e32 v108, 0x3c000000, v110
	v_mul_f32_e32 v109, 0x3c000000, v111
	v_mul_f32_e32 v105, 0x3c000000, v105
	v_cvt_pk_fp8_f32 v117, v108, v109 op_sel:[0,0,1]
	v_mul_f32_e32 v108, 0x3c000000, v104
	v_mov_b32_e32 v104, v3
	v_cvt_pk_fp8_f32 v104, v108, v105
	v_mul_f32_e32 v96, 0x3c000000, v96
	v_mul_f32_e32 v97, 0x3c000000, v97
	v_mov_b32_e32 v105, v3
	v_cvt_pk_fp8_f32 v105, v96, v97
	v_mul_f32_e32 v96, 0x3c000000, v98
	v_mul_f32_e32 v97, 0x3c000000, v99
	v_mul_f32_e32 v99, 0x3c000000, v100
	v_mul_f32_e32 v100, 0x3c000000, v101
	v_mov_b32_e32 v98, v3
	v_cvt_pk_fp8_f32 v98, v99, v100
	v_mul_f32_e32 v92, 0x3c000000, v92
	v_mul_f32_e32 v93, 0x3c000000, v93
	v_mov_b32_e32 v99, v3
	v_cvt_pk_fp8_f32 v99, v92, v93
	v_mul_f32_e32 v92, 0x3c000000, v94
	v_mul_f32_e32 v93, 0x3c000000, v95
	v_mul_f32_e32 v89, 0x3c000000, v89
	v_cvt_pk_fp8_f32 v99, v92, v93 op_sel:[0,0,1]
	v_mul_f32_e32 v92, 0x3c000000, v88
	v_mov_b32_e32 v88, v3
	v_cvt_pk_fp8_f32 v88, v92, v89
	v_mul_f32_e32 v80, 0x3c000000, v80
	v_mul_f32_e32 v81, 0x3c000000, v81
	v_mov_b32_e32 v89, v3
	v_cvt_pk_fp8_f32 v89, v80, v81
	v_mul_f32_e32 v80, 0x3c000000, v82
	v_mul_f32_e32 v81, 0x3c000000, v83
	v_mul_f32_e32 v83, 0x3c000000, v84
	v_mul_f32_e32 v84, 0x3c000000, v85
	v_mov_b32_e32 v82, v3
	v_cvt_pk_fp8_f32 v82, v83, v84
	v_mul_f32_e32 v76, 0x3c000000, v76
	v_mul_f32_e32 v77, 0x3c000000, v77
	v_mov_b32_e32 v83, v3
	v_cvt_pk_fp8_f32 v83, v76, v77
	v_mul_f32_e32 v76, 0x3c000000, v78
	v_mul_f32_e32 v77, 0x3c000000, v79
	v_mul_f32_e32 v73, 0x3c000000, v73
	v_cvt_pk_fp8_f32 v83, v76, v77 op_sel:[0,0,1]
	v_mul_f32_e32 v76, 0x3c000000, v72
	v_mov_b32_e32 v72, v3
	v_cvt_pk_fp8_f32 v72, v76, v73
	v_mul_f32_e32 v68, 0x3c000000, v68
	v_mul_f32_e32 v69, 0x3c000000, v69
	v_mov_b32_e32 v73, v3
	v_cvt_pk_fp8_f32 v73, v68, v69
	v_mul_f32_e32 v68, 0x3c000000, v70
	v_mul_f32_e32 v70, 0x3c000000, v64
	v_mul_f32_e32 v65, 0x3c000000, v65
	v_mov_b32_e32 v64, v3
	v_cvt_pk_fp8_f32 v64, v70, v65
	v_mul_f32_e32 v60, 0x3c000000, v60
	v_mul_f32_e32 v61, 0x3c000000, v61
	v_mov_b32_e32 v65, v3
	v_cvt_pk_fp8_f32 v65, v60, v61
	v_mul_f32_e32 v60, 0x3c000000, v62
	v_mul_f32_e32 v61, 0x3c000000, v63
	v_mul_f32_e32 v57, 0x3c000000, v57
	v_cvt_pk_fp8_f32 v65, v60, v61 op_sel:[0,0,1]
	v_mul_f32_e32 v60, 0x3c000000, v56
	v_mov_b32_e32 v56, v3
	v_cvt_pk_fp8_f32 v56, v60, v57
	v_mul_f32_e32 v48, 0x3c000000, v48
	v_mul_f32_e32 v49, 0x3c000000, v49
	v_mov_b32_e32 v57, v3
	v_cvt_pk_fp8_f32 v57, v48, v49
	v_mul_f32_e32 v48, 0x3c000000, v50
	v_mul_f32_e32 v49, 0x3c000000, v51
	v_mul_f32_e32 v51, 0x3c000000, v52
	v_mul_f32_e32 v52, 0x3c000000, v53
	v_mov_b32_e32 v50, v3
	v_cvt_pk_fp8_f32 v50, v51, v52
	v_mul_f32_e32 v44, 0x3c000000, v44
	v_mul_f32_e32 v45, 0x3c000000, v45
	v_mov_b32_e32 v51, v3
	v_cvt_pk_fp8_f32 v51, v44, v45
	v_mul_f32_e32 v44, 0x3c000000, v46
	v_mul_f32_e32 v45, 0x3c000000, v47
	v_mul_f32_e32 v41, 0x3c000000, v41
	v_cvt_pk_fp8_f32 v51, v44, v45 op_sel:[0,0,1]
	v_mul_f32_e32 v44, 0x3c000000, v40
	v_mov_b32_e32 v40, v3
	v_cvt_pk_fp8_f32 v40, v44, v41
	v_mul_f32_e32 v32, 0x3c000000, v32
	v_mul_f32_e32 v33, 0x3c000000, v33
	v_mov_b32_e32 v41, v3
	v_cvt_pk_fp8_f32 v41, v32, v33
	v_mul_f32_e32 v32, 0x3c000000, v34
	v_mul_f32_e32 v33, 0x3c000000, v35
	v_mul_f32_e32 v35, 0x3c000000, v36
	v_mul_f32_e32 v36, 0x3c000000, v37
	v_mov_b32_e32 v34, v3
	v_cvt_pk_fp8_f32 v34, v35, v36
	v_mul_f32_e32 v28, 0x3c000000, v28
	v_mul_f32_e32 v29, 0x3c000000, v29
	v_mov_b32_e32 v35, v3
	v_cvt_pk_fp8_f32 v35, v28, v29
	v_mul_f32_e32 v28, 0x3c000000, v30
	v_mul_f32_e32 v29, 0x3c000000, v31
	v_mul_f32_e32 v25, 0x3c000000, v25
	v_cvt_pk_fp8_f32 v35, v28, v29 op_sel:[0,0,1]
	v_mul_f32_e32 v28, 0x3c000000, v24
	v_mov_b32_e32 v24, v3
	v_mul_f32_e32 v118, 0x3c000000, v118
	v_mul_f32_e32 v119, 0x3c000000, v119
	v_cvt_pk_fp8_f32 v24, v28, v25
	v_mul_f32_e32 v16, 0x3c000000, v16
	v_mul_f32_e32 v17, 0x3c000000, v17
	v_mov_b32_e32 v25, v3
	v_or_b32_e32 v114, 16, v148
	v_cvt_pk_fp8_f32 v116, v118, v119 op_sel:[0,0,1]
	v_mul_f32_e32 v106, 0x3c000000, v106
	v_mul_f32_e32 v107, 0x3c000000, v107
	v_cvt_pk_fp8_f32 v25, v16, v17
	v_mul_f32_e32 v16, 0x3c000000, v18
	v_mul_f32_e32 v17, 0x3c000000, v19
	v_mul_f32_e32 v19, 0x3c000000, v20
	v_mul_f32_e32 v20, 0x3c000000, v21
	v_mov_b32_e32 v18, v3
	v_ashrrev_i32_e32 v115, 31, v114
	v_cvt_pk_fp8_f32 v104, v106, v107 op_sel:[0,0,1]
	v_cvt_pk_fp8_f32 v105, v96, v97 op_sel:[0,0,1]
	v_cvt_pk_fp8_f32 v18, v19, v20
	v_mul_f32_e32 v12, 0x3c000000, v12
	v_mul_f32_e32 v13, 0x3c000000, v13
	v_mov_b32_e32 v19, v3
	v_lshlrev_b64 v[96:97], 11, v[114:115]
	v_cvt_pk_fp8_f32 v19, v12, v13
	v_lshl_add_u64 v[96:97], v[150:151], 0, v[96:97]
	v_mul_f32_e32 v100, 0x3c000000, v102
	v_mul_f32_e32 v101, 0x3c000000, v103
	global_store_dwordx2 v[96:97], v[116:117], off
	global_store_dwordx2 v[96:97], v[104:105], off offset:128
	v_or_b32_e32 v96, 32, v148
	v_cvt_pk_fp8_f32 v98, v100, v101 op_sel:[0,0,1]
	v_mul_f32_e32 v90, 0x3c000000, v90
	v_mul_f32_e32 v91, 0x3c000000, v91
	v_ashrrev_i32_e32 v97, 31, v96
	v_cvt_pk_fp8_f32 v88, v90, v91 op_sel:[0,0,1]
	v_cvt_pk_fp8_f32 v89, v80, v81 op_sel:[0,0,1]
	s_mov_b32 s5, 0x40000
	v_mul_f32_e32 v12, 0x3c000000, v14
	v_mul_f32_e32 v13, 0x3c000000, v15
	v_lshlrev_b64 v[80:81], 11, v[96:97]
	v_cvt_pk_fp8_f32 v57, v48, v49 op_sel:[0,0,1]
	v_add_co_u32_e32 v48, vcc, s5, v112
	v_cvt_pk_fp8_f32 v19, v12, v13 op_sel:[0,0,1]
	v_mul_f32_e32 v12, 0x3c000000, v8
	v_mul_f32_e32 v9, 0x3c000000, v9
	v_mov_b32_e32 v8, v3
	v_lshl_add_u64 v[80:81], v[150:151], 0, v[80:81]
	v_mul_f32_e32 v84, 0x3c000000, v86
	v_mul_f32_e32 v85, 0x3c000000, v87
	v_addc_co_u32_e32 v49, vcc, 0, v113, vcc
	s_mov_b32 s5, 0x48000
	v_cvt_pk_fp8_f32 v8, v12, v9
	v_mul_f32_e32 v4, 0x3c000000, v4
	v_mul_f32_e32 v5, 0x3c000000, v5
	v_mov_b32_e32 v9, v3
	global_store_dwordx2 v[80:81], v[98:99], off
	global_store_dwordx2 v[80:81], v[88:89], off offset:128
	v_or_b32_e32 v80, 48, v148
	v_cvt_pk_fp8_f32 v82, v84, v85 op_sel:[0,0,1]
	v_mul_f32_e32 v74, 0x3c000000, v74
	v_mul_f32_e32 v75, 0x3c000000, v75
	v_mul_f32_e32 v69, 0x3c000000, v71
	v_mul_f32_e32 v66, 0x3c000000, v66
	v_mul_f32_e32 v67, 0x3c000000, v67
	v_cvt_pk_fp8_f32 v41, v32, v33 op_sel:[0,0,1]
	v_add_co_u32_e32 v32, vcc, s5, v112
	v_cvt_pk_fp8_f32 v9, v4, v5
	v_ashrrev_i32_e32 v81, 31, v80
	v_cvt_pk_fp8_f32 v72, v74, v75 op_sel:[0,0,1]
	v_cvt_pk_fp8_f32 v73, v68, v69 op_sel:[0,0,1]
	v_cvt_pk_fp8_f32 v64, v66, v67 op_sel:[0,0,1]
	v_mul_f32_e32 v58, 0x3c000000, v58
	v_mul_f32_e32 v59, 0x3c000000, v59
	v_mul_f32_e32 v52, 0x3c000000, v54
	v_mul_f32_e32 v53, 0x3c000000, v55
	v_addc_co_u32_e32 v33, vcc, 0, v113, vcc
	s_mov_b32 s5, 0x50000
	v_lshlrev_b64 v[68:69], 11, v[80:81]
	v_cvt_pk_fp8_f32 v56, v58, v59 op_sel:[0,0,1]
	v_cvt_pk_fp8_f32 v50, v52, v53 op_sel:[0,0,1]
	v_mul_f32_e32 v42, 0x3c000000, v42
	v_mul_f32_e32 v43, 0x3c000000, v43
	v_mul_f32_e32 v36, 0x3c000000, v38
	v_mul_f32_e32 v37, 0x3c000000, v39
	v_cvt_pk_fp8_f32 v25, v16, v17 op_sel:[0,0,1]
	v_add_co_u32_e32 v16, vcc, s5, v112
	v_mul_f32_e32 v20, 0x3c000000, v22
	v_mul_f32_e32 v21, 0x3c000000, v23
	v_lshl_add_u64 v[68:69], v[150:151], 0, v[68:69]
	s_mov_b64 s[8:9], 0x40000
	v_cvt_pk_fp8_f32 v40, v42, v43 op_sel:[0,0,1]
	v_cvt_pk_fp8_f32 v34, v36, v37 op_sel:[0,0,1]
	v_mul_f32_e32 v26, 0x3c000000, v26
	v_mul_f32_e32 v27, 0x3c000000, v27
	v_addc_co_u32_e32 v17, vcc, 0, v113, vcc
	v_cvt_pk_fp8_f32 v18, v20, v21 op_sel:[0,0,1]
	v_mul_f32_e32 v10, 0x3c000000, v10
	v_mul_f32_e32 v11, 0x3c000000, v11
	v_mul_f32_e32 v4, 0x3c000000, v6
	v_mul_f32_e32 v5, 0x3c000000, v7
	s_mov_b32 s5, 0x58000
	global_store_dwordx2 v[68:69], v[82:83], off
	global_store_dwordx2 v[68:69], v[72:73], off offset:128
	v_lshl_add_u64 v[68:69], v[112:113], 0, s[8:9]
	s_mov_b64 s[8:9], 0x48000
	v_cvt_pk_fp8_f32 v24, v26, v27 op_sel:[0,0,1]
	v_cvt_pk_fp8_f32 v8, v10, v11 op_sel:[0,0,1]
	v_cvt_pk_fp8_f32 v9, v4, v5 op_sel:[0,0,1]
	v_add_co_u32_e32 v4, vcc, s5, v112
	global_store_dwordx2 v[48:49], v[64:65], off
	global_store_dwordx2 v[68:69], v[56:57], off offset:128
	v_lshl_add_u64 v[48:49], v[112:113], 0, s[8:9]
	s_mov_b64 s[8:9], 0x50000
	v_addc_co_u32_e32 v5, vcc, 0, v113, vcc
	global_store_dwordx2 v[32:33], v[50:51], off
	global_store_dwordx2 v[48:49], v[40:41], off offset:128
	v_lshl_add_u64 v[32:33], v[112:113], 0, s[8:9]
	s_mov_b64 s[8:9], 0x58000
	s_and_b64 vcc, exec, s[40:41]
	s_mov_b32 s44, s4
	s_mov_b32 s50, s42
	s_mov_b64 s[54:55], s[52:53]
	s_mov_b64 s[56:57], s[46:47]
	global_store_dwordx2 v[16:17], v[34:35], off
	global_store_dwordx2 v[32:33], v[24:25], off offset:128
	v_lshl_add_u64 v[16:17], v[112:113], 0, s[8:9]
	global_store_dwordx2 v[4:5], v[18:19], off
	global_store_dwordx2 v[16:17], v[8:9], off offset:128
	s_cbranch_vccz .LBB0_427
	s_waitcnt vmcnt(0)
	v_readlane_b32 s86, v253, 23
	v_readlane_b32 s88, v253, 25
	s_cmpk_gt_u32 s27, 0xff
	v_readlane_b32 s84, v253, 20
	v_readlane_b32 s76, v253, 22
	v_readlane_b32 s87, v253, 24
	v_readlane_b32 s89, v253, 26
	v_readlane_b32 s85, v253, 21
	s_cbranch_scc1 .LBB0_434
	s_barrier

.LBB0_605:
	s_add_u32 s56, s54, 0x80
	s_addc_u32 s57, s55, 0
	s_add_i32 vcc_lo, 0, 0x10000
	v_add_u32_e32 v220, vcc_lo, v145
	v_add_u32_e32 v221, vcc_lo, v146
	ds_read_b128 v[222:225], v220
	ds_read_b128 v[230:233], v220 offset:2048
	ds_read_b128 v[226:229], v221
	ds_read_b128 v[234:237], v221 offset:2048
	s_cmp_eq_u32 s97, 12
	s_cselect_b32 s59, s45, s57
	s_cselect_b32 s58, s47, s56
	s_cselect_b32 s57, s8, s96
	s_cselect_b32 s56, s9, s89
	s_add_i32 s76, s31, s64
	v_lshl_add_u64 v[142:143], s[54:55], 0, v[140:141]
	s_mov_b32 m0, s76
	ds_read_b128 v[166:169], v148
	ds_read_b128 v[182:185], v148 offset:2048
	ds_read_b128 v[170:173], v149
	ds_read_b128 v[186:189], v149 offset:2048
	ds_read_b128 v[190:193], v148 offset:4096
	ds_read_b128 v[198:201], v148 offset:6144
	ds_read_b128 v[194:197], v149 offset:4096
	ds_read_b128 v[202:205], v149 offset:6144
	global_load_lds_dwordx4 v[142:143], off
	v_lshl_add_u64 v[142:143], s[54:55], 0, v[138:139]
	s_add_i32 m0, s76, 0x2000
	s_nop 0
	global_load_lds_dwordx4 v[142:143], off
	s_waitcnt vmcnt(6)
	s_waitcnt lgkmcnt(0)
	s_barrier
	s_setprio 1
	s_waitcnt lgkmcnt(0)
	v_mfma_f32_16x16x128_f8f6f4 v[128:131], v[222:229], v[166:173], v[128:131]
	v_mfma_f32_16x16x128_f8f6f4 v[124:127], v[230:237], v[166:173], v[124:127]
	v_mfma_f32_16x16x128_f8f6f4 v[120:123], v[222:229], v[182:189], v[120:123]
	v_mfma_f32_16x16x128_f8f6f4 v[112:115], v[230:237], v[182:189], v[112:115]
	v_mfma_f32_16x16x128_f8f6f4 v[104:107], v[222:229], v[190:197], v[104:107]
	v_mfma_f32_16x16x128_f8f6f4 v[96:99], v[230:237], v[190:197], v[96:99]
	v_mfma_f32_16x16x128_f8f6f4 v[88:91], v[222:229], v[198:205], v[88:91]
	v_mfma_f32_16x16x128_f8f6f4 v[80:83], v[230:237], v[198:205], v[80:83]
	s_setprio 0
	s_barrier
	s_add_i32 s76, 0, 0x14000
	v_add_u32_e32 v142, s76, v145
	v_add_u32_e32 v143, s76, v146
	s_mov_b32 m0, s5
	ds_read_b128 v[150:153], v142
	ds_read_b128 v[158:161], v142 offset:2048
	ds_read_b128 v[154:157], v143
	ds_read_b128 v[162:165], v143 offset:2048
	v_lshl_add_u64 v[142:143], s[56:57], 0, v[2:3]
	global_load_lds_dwordx4 v[142:143], off
	v_lshl_add_u64 v[174:175], s[56:57], 0, v[134:135]
	s_mov_b32 m0, s43
	s_nop 0
	global_load_lds_dwordx4 v[174:175], off
	s_waitcnt vmcnt(6)
	s_waitcnt lgkmcnt(0)
	s_barrier
	s_setprio 1
	s_waitcnt lgkmcnt(0)
	v_mfma_f32_16x16x128_f8f6f4 v[116:119], v[150:157], v[166:173], v[116:119]
	v_mfma_f32_16x16x128_f8f6f4 v[108:111], v[158:165], v[166:173], v[108:111]
	v_mfma_f32_16x16x128_f8f6f4 v[100:103], v[150:157], v[182:189], v[100:103]
	v_mfma_f32_16x16x128_f8f6f4 v[92:95], v[158:165], v[182:189], v[92:95]
	v_mfma_f32_16x16x128_f8f6f4 v[84:87], v[150:157], v[190:197], v[84:87]
	v_mfma_f32_16x16x128_f8f6f4 v[76:79], v[158:165], v[190:197], v[76:79]
	v_mfma_f32_16x16x128_f8f6f4 v[72:75], v[150:157], v[198:205], v[72:75]
	v_mfma_f32_16x16x128_f8f6f4 v[68:71], v[158:165], v[198:205], v[68:71]
	s_setprio 0
	s_barrier
	s_add_u32 s80, s58, 0x40000
	s_addc_u32 s81, s59, 0
	s_add_i32 s76, s76, s64
	v_lshl_add_u64 v[176:177], s[80:81], 0, v[136:137]
	s_mov_b32 m0, s76
	ds_read_b128 v[166:169], v148 offset:16384
	ds_read_b128 v[182:185], v148 offset:18432
	ds_read_b128 v[170:173], v149 offset:16384
	ds_read_b128 v[186:189], v149 offset:18432
	ds_read_b128 v[190:193], v148 offset:20480
	ds_read_b128 v[198:201], v148 offset:22528
	ds_read_b128 v[194:197], v149 offset:20480
	ds_read_b128 v[202:205], v149 offset:22528
	global_load_lds_dwordx4 v[176:177], off
	v_lshl_add_u64 v[176:177], s[80:81], 0, v[132:133]
	s_add_i32 m0, s76, 0x2000
	s_nop 0
	global_load_lds_dwordx4 v[176:177], off
	s_waitcnt vmcnt(6)
	s_waitcnt lgkmcnt(0)
	s_barrier
	s_setprio 1
	s_waitcnt lgkmcnt(0)
	v_mfma_f32_16x16x128_f8f6f4 v[52:55], v[150:157], v[166:173], v[52:55]
	v_mfma_f32_16x16x128_f8f6f4 v[44:47], v[158:165], v[166:173], v[44:47]
	v_mfma_f32_16x16x128_f8f6f4 v[36:39], v[150:157], v[182:189], v[36:39]
	v_mfma_f32_16x16x128_f8f6f4 v[28:31], v[158:165], v[182:189], v[28:31]
	v_mfma_f32_16x16x128_f8f6f4 v[20:23], v[150:157], v[190:197], v[20:23]
	v_mfma_f32_16x16x128_f8f6f4 v[12:15], v[158:165], v[190:197], v[12:15]
	v_mfma_f32_16x16x128_f8f6f4 v[8:11], v[150:157], v[198:205], v[8:11]
	v_mfma_f32_16x16x128_f8f6f4 v[4:7], v[158:165], v[198:205], v[4:7]
	s_setprio 0
	s_barrier
	s_add_u32 s80, s56, 0x40000
	s_addc_u32 s81, s57, 0
	s_mov_b32 m0, s66
	v_lshl_add_u64 v[176:177], s[80:81], 0, v[2:3]
	global_load_lds_dwordx4 v[176:177], off
	v_lshl_add_u64 v[176:177], s[80:81], 0, v[134:135]
	s_mov_b32 m0, s67
	s_nop 0
	global_load_lds_dwordx4 v[176:177], off
	s_waitcnt vmcnt(6)
	s_waitcnt lgkmcnt(0)
	s_barrier
	s_setprio 1
	s_waitcnt lgkmcnt(0)
	v_mfma_f32_16x16x128_f8f6f4 v[64:67], v[222:229], v[166:173], v[64:67]
	v_mfma_f32_16x16x128_f8f6f4 v[60:63], v[230:237], v[166:173], v[60:63]
	v_mfma_f32_16x16x128_f8f6f4 v[56:59], v[222:229], v[182:189], v[56:59]
	v_mfma_f32_16x16x128_f8f6f4 v[48:51], v[230:237], v[182:189], v[48:51]
	v_mfma_f32_16x16x128_f8f6f4 v[40:43], v[222:229], v[190:197], v[40:43]
	v_mfma_f32_16x16x128_f8f6f4 v[32:35], v[230:237], v[190:197], v[32:35]
	v_mfma_f32_16x16x128_f8f6f4 v[24:27], v[222:229], v[198:205], v[24:27]
	v_mfma_f32_16x16x128_f8f6f4 v[16:19], v[230:237], v[198:205], v[16:19]
	s_setprio 0
	s_barrier
	v_add_u32_e32 v220, s31, v145
	v_add_u32_e32 v221, s31, v146
	ds_read_b128 v[222:225], v220
	ds_read_b128 v[230:233], v220 offset:2048
	ds_read_b128 v[226:229], v221
	ds_read_b128 v[234:237], v221 offset:2048
	s_add_i32 s76, vcc_lo, s64
	v_lshl_add_u64 v[176:177], s[58:59], 0, v[136:137]
	s_mov_b32 m0, s76
	ds_read_b128 v[166:169], v148 offset:32768
	ds_read_b128 v[182:185], v148 offset:34816
	ds_read_b128 v[170:173], v149 offset:32768
	ds_read_b128 v[186:189], v149 offset:34816
	ds_read_b128 v[190:193], v148 offset:36864
	ds_read_b128 v[198:201], v148 offset:38912
	ds_read_b128 v[194:197], v149 offset:36864
	ds_read_b128 v[202:205], v149 offset:38912
	global_load_lds_dwordx4 v[176:177], off
	v_lshl_add_u64 v[176:177], s[58:59], 0, v[132:133]
	s_add_i32 m0, s76, 0x2000
	s_nop 0
	global_load_lds_dwordx4 v[176:177], off
	s_waitcnt vmcnt(6)
	s_waitcnt lgkmcnt(0)
	s_barrier
	s_setprio 1
	s_waitcnt lgkmcnt(0)
	v_mfma_f32_16x16x128_f8f6f4 v[128:131], v[222:229], v[166:173], v[128:131]
	v_mfma_f32_16x16x128_f8f6f4 v[124:127], v[230:237], v[166:173], v[124:127]
	v_mfma_f32_16x16x128_f8f6f4 v[120:123], v[222:229], v[182:189], v[120:123]
	v_mfma_f32_16x16x128_f8f6f4 v[112:115], v[230:237], v[182:189], v[112:115]
	v_mfma_f32_16x16x128_f8f6f4 v[104:107], v[222:229], v[190:197], v[104:107]
	v_mfma_f32_16x16x128_f8f6f4 v[96:99], v[230:237], v[190:197], v[96:99]
	v_mfma_f32_16x16x128_f8f6f4 v[88:91], v[222:229], v[198:205], v[88:91]
	v_mfma_f32_16x16x128_f8f6f4 v[80:83], v[230:237], v[198:205], v[80:83]
	s_setprio 0
	s_barrier
	s_add_i32 s76, 0, 0x1c000
	s_mov_b32 m0, s72
	v_add_u32_e32 v154, s76, v145
	v_add_u32_e32 v162, s76, v146
	v_lshl_add_u64 v[142:143], v[142:143], 0, s[20:21]
	ds_read_b128 v[150:153], v154
	ds_read_b128 v[158:161], v154 offset:2048
	ds_read_b128 v[154:157], v162
	ds_read_b128 v[162:165], v162 offset:2048
	global_load_lds_dwordx4 v[142:143], off
	v_lshl_add_u64 v[142:143], v[174:175], 0, s[20:21]
	s_mov_b32 m0, s73
	s_nop 0
	global_load_lds_dwordx4 v[142:143], off
	s_waitcnt vmcnt(6)
	s_waitcnt lgkmcnt(0)
	s_barrier
	s_setprio 1
	s_waitcnt lgkmcnt(0)
	v_mfma_f32_16x16x128_f8f6f4 v[116:119], v[150:157], v[166:173], v[116:119]
	v_mfma_f32_16x16x128_f8f6f4 v[108:111], v[158:165], v[166:173], v[108:111]
	v_mfma_f32_16x16x128_f8f6f4 v[100:103], v[150:157], v[182:189], v[100:103]
	v_mfma_f32_16x16x128_f8f6f4 v[92:95], v[158:165], v[182:189], v[92:95]
	v_mfma_f32_16x16x128_f8f6f4 v[84:87], v[150:157], v[190:197], v[84:87]
	v_mfma_f32_16x16x128_f8f6f4 v[76:79], v[158:165], v[190:197], v[76:79]
	v_mfma_f32_16x16x128_f8f6f4 v[72:75], v[150:157], v[198:205], v[72:75]
	v_mfma_f32_16x16x128_f8f6f4 v[68:71], v[158:165], v[198:205], v[68:71]
	s_setprio 0
	s_barrier
	s_add_u32 s58, s58, 0x40080
	s_addc_u32 s59, s59, 0
	s_add_i32 s76, s76, s64
	v_lshl_add_u64 v[142:143], s[58:59], 0, v[136:137]
	s_mov_b32 m0, s76
	ds_read_b128 v[166:169], v148 offset:49152
	ds_read_b128 v[182:185], v148 offset:51200
	ds_read_b128 v[170:173], v149 offset:49152
	ds_read_b128 v[186:189], v149 offset:51200
	ds_read_b128 v[190:193], v148 offset:53248
	ds_read_b128 v[198:201], v148 offset:55296
	ds_read_b128 v[194:197], v149 offset:53248
	ds_read_b128 v[202:205], v149 offset:55296
	global_load_lds_dwordx4 v[142:143], off
	v_lshl_add_u64 v[142:143], s[58:59], 0, v[132:133]
	s_add_i32 m0, s76, 0x2000
	s_nop 0
	global_load_lds_dwordx4 v[142:143], off
	s_waitcnt vmcnt(6)
	s_waitcnt lgkmcnt(0)
	s_barrier
	s_setprio 1
	s_waitcnt lgkmcnt(0)
	v_mfma_f32_16x16x128_f8f6f4 v[52:55], v[150:157], v[166:173], v[52:55]
	v_mfma_f32_16x16x128_f8f6f4 v[44:47], v[158:165], v[166:173], v[44:47]
	v_mfma_f32_16x16x128_f8f6f4 v[36:39], v[150:157], v[182:189], v[36:39]
	v_mfma_f32_16x16x128_f8f6f4 v[28:31], v[158:165], v[182:189], v[28:31]
	v_mfma_f32_16x16x128_f8f6f4 v[20:23], v[150:157], v[190:197], v[20:23]
	v_mfma_f32_16x16x128_f8f6f4 v[12:15], v[158:165], v[190:197], v[12:15]
	v_mfma_f32_16x16x128_f8f6f4 v[8:11], v[150:157], v[198:205], v[8:11]
	v_mfma_f32_16x16x128_f8f6f4 v[4:7], v[158:165], v[198:205], v[4:7]
	s_setprio 0
	s_barrier
	s_add_u32 s56, s56, 0x40080
	s_addc_u32 s57, s57, 0
	s_mov_b32 m0, s74
	v_lshl_add_u64 v[142:143], s[56:57], 0, v[2:3]
	global_load_lds_dwordx4 v[142:143], off
	v_lshl_add_u64 v[142:143], s[56:57], 0, v[134:135]
	s_mov_b32 m0, s75
	s_nop 0
	global_load_lds_dwordx4 v[142:143], off
	s_waitcnt vmcnt(6)
	s_waitcnt lgkmcnt(0)
	s_barrier
	s_setprio 1
	s_waitcnt lgkmcnt(0)
	v_mfma_f32_16x16x128_f8f6f4 v[64:67], v[222:229], v[166:173], v[64:67]
	v_mfma_f32_16x16x128_f8f6f4 v[60:63], v[230:237], v[166:173], v[60:63]
	v_mfma_f32_16x16x128_f8f6f4 v[56:59], v[222:229], v[182:189], v[56:59]
	v_mfma_f32_16x16x128_f8f6f4 v[48:51], v[230:237], v[182:189], v[48:51]
	v_mfma_f32_16x16x128_f8f6f4 v[40:43], v[222:229], v[190:197], v[40:43]
	v_mfma_f32_16x16x128_f8f6f4 v[32:35], v[230:237], v[190:197], v[32:35]
	v_mfma_f32_16x16x128_f8f6f4 v[24:27], v[222:229], v[198:205], v[24:27]
	v_mfma_f32_16x16x128_f8f6f4 v[16:19], v[230:237], v[198:205], v[16:19]
	s_setprio 0
	s_barrier
	s_add_i32 s97, s97, 2
	s_add_u32 s89, s89, 0x100
	s_addc_u32 s96, s96, 0
	s_add_u32 s54, s54, 0x100
	s_addc_u32 s55, s55, 0
	s_cmp_gt_u32 s97, 13
	s_cbranch_scc0 .LBB0_605
	v_lshl_add_u32 v150, s42, 8, v144
	v_lshl_or_b32 v142, s4, 8, v147
	v_ashrrev_i32_e32 v151, 31, v150
	v_ashrrev_i32_e32 v143, 31, v142
	v_lshlrev_b64 v[152:153], 12, v[150:151]
	v_lshl_add_u64 v[152:153], s[0:1], 0, v[152:153]
	v_lshlrev_b64 v[154:155], 1, v[142:143]
	v_lshl_add_u64 v[142:143], v[152:153], 0, v[154:155]
	v_pk_mul_f32 v[130:131], v[130:131], s[22:23] op_sel_hi:[1,0]
	v_pk_mul_f32 v[128:129], v[128:129], s[22:23] op_sel_hi:[1,0]
	v_pk_mul_f32 v[152:153], v[126:127], s[22:23] op_sel_hi:[1,0]
	v_pk_mul_f32 v[126:127], v[124:125], s[22:23] op_sel_hi:[1,0]
	v_cvt_pk_bf16_f32 v124, v128, v129
	v_cvt_pk_bf16_f32 v125, v130, v131
	v_cvt_pk_bf16_f32 v126, v126, v127
	v_cvt_pk_bf16_f32 v127, v152, v153
	global_store_dwordx4 v[142:143], v[124:127], off
	v_pk_mul_f32 v[118:119], v[118:119], s[22:23] op_sel_hi:[1,0]
	v_pk_mul_f32 v[116:117], v[116:117], s[22:23] op_sel_hi:[1,0]
	v_pk_mul_f32 v[124:125], v[110:111], s[22:23] op_sel_hi:[1,0]
	v_pk_mul_f32 v[110:111], v[108:109], s[22:23] op_sel_hi:[1,0]
	v_cvt_pk_bf16_f32 v108, v116, v117
	v_cvt_pk_bf16_f32 v109, v118, v119
	v_cvt_pk_bf16_f32 v110, v110, v111
	v_cvt_pk_bf16_f32 v111, v124, v125
	global_store_dwordx4 v[142:143], v[108:111], off offset:256
	v_pk_mul_f32 v[114:115], v[114:115], s[22:23] op_sel_hi:[1,0]
	v_pk_mul_f32 v[112:113], v[112:113], s[22:23] op_sel_hi:[1,0]
	v_or_b32_e32 v108, 16, v150
	v_ashrrev_i32_e32 v109, 31, v108
	v_lshlrev_b64 v[108:109], 12, v[108:109]
	v_lshl_add_u64 v[108:109], s[0:1], 0, v[108:109]
	v_lshl_add_u64 v[116:117], v[108:109], 0, v[154:155]
	v_pk_mul_f32 v[110:111], v[122:123], s[22:23] op_sel_hi:[1,0]
	v_pk_mul_f32 v[108:109], v[120:121], s[22:23] op_sel_hi:[1,0]
	v_pk_mul_f32 v[102:103], v[102:103], s[22:23] op_sel_hi:[1,0]
	v_cvt_pk_bf16_f32 v108, v108, v109
	v_cvt_pk_bf16_f32 v109, v110, v111
	v_cvt_pk_bf16_f32 v110, v112, v113
	v_cvt_pk_bf16_f32 v111, v114, v115
	global_store_dwordx4 v[116:117], v[108:111], off
	v_pk_mul_f32 v[100:101], v[100:101], s[22:23] op_sel_hi:[1,0]
	v_pk_mul_f32 v[98:99], v[98:99], s[22:23] op_sel_hi:[1,0]
	v_pk_mul_f32 v[108:109], v[94:95], s[22:23] op_sel_hi:[1,0]
	v_pk_mul_f32 v[94:95], v[92:93], s[22:23] op_sel_hi:[1,0]
	v_cvt_pk_bf16_f32 v92, v100, v101
	v_cvt_pk_bf16_f32 v93, v102, v103
	v_cvt_pk_bf16_f32 v94, v94, v95
	v_cvt_pk_bf16_f32 v95, v108, v109
	global_store_dwordx4 v[116:117], v[92:95], off offset:256
	v_pk_mul_f32 v[96:97], v[96:97], s[22:23] op_sel_hi:[1,0]
	v_pk_mul_f32 v[86:87], v[86:87], s[22:23] op_sel_hi:[1,0]
	v_or_b32_e32 v92, 32, v150
	v_ashrrev_i32_e32 v93, 31, v92
	v_lshlrev_b64 v[92:93], 12, v[92:93]
	v_lshl_add_u64 v[92:93], s[0:1], 0, v[92:93]
	v_lshl_add_u64 v[100:101], v[92:93], 0, v[154:155]
	v_pk_mul_f32 v[94:95], v[106:107], s[22:23] op_sel_hi:[1,0]
	v_pk_mul_f32 v[92:93], v[104:105], s[22:23] op_sel_hi:[1,0]
	v_pk_mul_f32 v[84:85], v[84:85], s[22:23] op_sel_hi:[1,0]
	v_cvt_pk_bf16_f32 v92, v92, v93
	v_cvt_pk_bf16_f32 v93, v94, v95
	v_cvt_pk_bf16_f32 v94, v96, v97
	v_cvt_pk_bf16_f32 v95, v98, v99
	global_store_dwordx4 v[100:101], v[92:95], off
	v_pk_mul_f32 v[82:83], v[82:83], s[22:23] op_sel_hi:[1,0]
	v_pk_mul_f32 v[80:81], v[80:81], s[22:23] op_sel_hi:[1,0]
	v_pk_mul_f32 v[92:93], v[78:79], s[22:23] op_sel_hi:[1,0]
	v_pk_mul_f32 v[78:79], v[76:77], s[22:23] op_sel_hi:[1,0]
	v_cvt_pk_bf16_f32 v76, v84, v85
	v_cvt_pk_bf16_f32 v77, v86, v87
	v_cvt_pk_bf16_f32 v78, v78, v79
	v_cvt_pk_bf16_f32 v79, v92, v93
	global_store_dwordx4 v[100:101], v[76:79], off offset:256
	v_pk_mul_f32 v[74:75], v[74:75], s[22:23] op_sel_hi:[1,0]
	v_pk_mul_f32 v[72:73], v[72:73], s[22:23] op_sel_hi:[1,0]
	v_or_b32_e32 v76, 48, v150
	v_ashrrev_i32_e32 v77, 31, v76
	v_lshlrev_b64 v[76:77], 12, v[76:77]
	v_lshl_add_u64 v[76:77], s[0:1], 0, v[76:77]
	v_lshl_add_u64 v[84:85], v[76:77], 0, v[154:155]
	v_pk_mul_f32 v[78:79], v[90:91], s[22:23] op_sel_hi:[1,0]
	v_pk_mul_f32 v[76:77], v[88:89], s[22:23] op_sel_hi:[1,0]
	v_pk_mul_f32 v[64:65], v[64:65], s[22:23] op_sel_hi:[1,0]
	v_cvt_pk_bf16_f32 v76, v76, v77
	v_cvt_pk_bf16_f32 v77, v78, v79
	v_cvt_pk_bf16_f32 v78, v80, v81
	v_cvt_pk_bf16_f32 v79, v82, v83
	global_store_dwordx4 v[84:85], v[76:79], off
	s_mov_b32 s4, 0x80000
	v_pk_mul_f32 v[66:67], v[66:67], s[22:23] op_sel_hi:[1,0]
	v_pk_mul_f32 v[76:77], v[70:71], s[22:23] op_sel_hi:[1,0]
	v_pk_mul_f32 v[70:71], v[68:69], s[22:23] op_sel_hi:[1,0]
	v_cvt_pk_bf16_f32 v68, v72, v73
	v_cvt_pk_bf16_f32 v69, v74, v75
	v_cvt_pk_bf16_f32 v70, v70, v71
	v_cvt_pk_bf16_f32 v71, v76, v77
	global_store_dwordx4 v[84:85], v[68:71], off offset:256
	s_mov_b64 s[8:9], 0x80000
	v_pk_mul_f32 v[54:55], v[54:55], s[22:23] op_sel_hi:[1,0]
	v_pk_mul_f32 v[70:71], v[62:63], s[22:23] op_sel_hi:[1,0]
	v_pk_mul_f32 v[62:63], v[60:61], s[22:23] op_sel_hi:[1,0]
	v_cvt_pk_bf16_f32 v60, v64, v65
	v_add_co_u32_e32 v64, vcc, s4, v142
	v_cvt_pk_bf16_f32 v61, v66, v67
	v_cvt_pk_bf16_f32 v62, v62, v63
	v_cvt_pk_bf16_f32 v63, v70, v71
	v_addc_co_u32_e32 v65, vcc, 0, v143, vcc
	global_store_dwordx4 v[64:65], v[60:63], off
	v_pk_mul_f32 v[52:53], v[52:53], s[22:23] op_sel_hi:[1,0]
	v_lshl_add_u64 v[68:69], v[142:143], 0, s[8:9]
	v_pk_mul_f32 v[60:61], v[46:47], s[22:23] op_sel_hi:[1,0]
	v_pk_mul_f32 v[46:47], v[44:45], s[22:23] op_sel_hi:[1,0]
	v_cvt_pk_bf16_f32 v44, v52, v53
	v_cvt_pk_bf16_f32 v45, v54, v55
	v_cvt_pk_bf16_f32 v46, v46, v47
	v_cvt_pk_bf16_f32 v47, v60, v61
	global_store_dwordx4 v[68:69], v[44:47], off offset:256
	v_pk_mul_f32 v[48:49], v[48:49], s[22:23] op_sel_hi:[1,0]
	s_mov_b32 s4, 0x90000
	v_pk_mul_f32 v[46:47], v[58:59], s[22:23] op_sel_hi:[1,0]
	v_pk_mul_f32 v[44:45], v[56:57], s[22:23] op_sel_hi:[1,0]
	v_pk_mul_f32 v[50:51], v[50:51], s[22:23] op_sel_hi:[1,0]
	v_cvt_pk_bf16_f32 v44, v44, v45
	v_cvt_pk_bf16_f32 v45, v46, v47
	v_cvt_pk_bf16_f32 v46, v48, v49
	v_add_co_u32_e32 v48, vcc, s4, v142
	v_cvt_pk_bf16_f32 v47, v50, v51
	s_nop 0
	v_addc_co_u32_e32 v49, vcc, 0, v143, vcc
	s_mov_b64 s[8:9], 0x90000
	global_store_dwordx4 v[48:49], v[44:47], off
	v_pk_mul_f32 v[38:39], v[38:39], s[22:23] op_sel_hi:[1,0]
	v_pk_mul_f32 v[36:37], v[36:37], s[22:23] op_sel_hi:[1,0]
	v_pk_mul_f32 v[44:45], v[30:31], s[22:23] op_sel_hi:[1,0]
	v_pk_mul_f32 v[30:31], v[28:29], s[22:23] op_sel_hi:[1,0]
	v_lshl_add_u64 v[52:53], v[142:143], 0, s[8:9]
	v_cvt_pk_bf16_f32 v28, v36, v37
	v_cvt_pk_bf16_f32 v29, v38, v39
	v_cvt_pk_bf16_f32 v30, v30, v31
	v_cvt_pk_bf16_f32 v31, v44, v45
	global_store_dwordx4 v[52:53], v[28:31], off offset:256
	v_pk_mul_f32 v[32:33], v[32:33], s[22:23] op_sel_hi:[1,0]
	s_mov_b32 s4, 0xa0000
	v_pk_mul_f32 v[30:31], v[42:43], s[22:23] op_sel_hi:[1,0]
	v_pk_mul_f32 v[28:29], v[40:41], s[22:23] op_sel_hi:[1,0]
	v_pk_mul_f32 v[34:35], v[34:35], s[22:23] op_sel_hi:[1,0]
	v_cvt_pk_bf16_f32 v28, v28, v29
	v_cvt_pk_bf16_f32 v29, v30, v31
	v_cvt_pk_bf16_f32 v30, v32, v33
	v_add_co_u32_e32 v32, vcc, s4, v142
	v_cvt_pk_bf16_f32 v31, v34, v35
	s_nop 0
	v_addc_co_u32_e32 v33, vcc, 0, v143, vcc
	s_mov_b64 s[8:9], 0xa0000
	global_store_dwordx4 v[32:33], v[28:31], off
	v_pk_mul_f32 v[22:23], v[22:23], s[22:23] op_sel_hi:[1,0]
	v_pk_mul_f32 v[20:21], v[20:21], s[22:23] op_sel_hi:[1,0]
	v_pk_mul_f32 v[28:29], v[14:15], s[22:23] op_sel_hi:[1,0]
	v_pk_mul_f32 v[14:15], v[12:13], s[22:23] op_sel_hi:[1,0]
	v_lshl_add_u64 v[36:37], v[142:143], 0, s[8:9]
	v_cvt_pk_bf16_f32 v12, v20, v21
	v_cvt_pk_bf16_f32 v13, v22, v23
	v_cvt_pk_bf16_f32 v14, v14, v15
	v_cvt_pk_bf16_f32 v15, v28, v29
	global_store_dwordx4 v[36:37], v[12:15], off offset:256
	v_pk_mul_f32 v[16:17], v[16:17], s[22:23] op_sel_hi:[1,0]
	s_mov_b32 s4, 0xb0000
	v_pk_mul_f32 v[14:15], v[26:27], s[22:23] op_sel_hi:[1,0]
	v_pk_mul_f32 v[12:13], v[24:25], s[22:23] op_sel_hi:[1,0]
	v_pk_mul_f32 v[18:19], v[18:19], s[22:23] op_sel_hi:[1,0]
	v_cvt_pk_bf16_f32 v12, v12, v13
	v_cvt_pk_bf16_f32 v13, v14, v15
	v_cvt_pk_bf16_f32 v14, v16, v17
	v_add_co_u32_e32 v16, vcc, s4, v142
	v_cvt_pk_bf16_f32 v15, v18, v19
	s_nop 0
	v_addc_co_u32_e32 v17, vcc, 0, v143, vcc
	s_mov_b64 s[8:9], 0xb0000
	global_store_dwordx4 v[16:17], v[12:15], off
	v_pk_mul_f32 v[10:11], v[10:11], s[22:23] op_sel_hi:[1,0]
	v_pk_mul_f32 v[8:9], v[8:9], s[22:23] op_sel_hi:[1,0]
	v_pk_mul_f32 v[12:13], v[6:7], s[22:23] op_sel_hi:[1,0]
	v_pk_mul_f32 v[6:7], v[4:5], s[22:23] op_sel_hi:[1,0]
	v_lshl_add_u64 v[20:21], v[142:143], 0, s[8:9]
	v_cvt_pk_bf16_f32 v4, v8, v9
	v_cvt_pk_bf16_f32 v5, v10, v11
	v_cvt_pk_bf16_f32 v6, v6, v7
	v_cvt_pk_bf16_f32 v7, v12, v13
	s_and_b64 vcc, exec, s[40:41]
	s_mov_b32 s4, s44
	s_mov_b32 s42, s46
	s_mov_b64 s[54:55], s[52:53]
	s_mov_b64 s[56:57], s[50:51]
	global_store_dwordx4 v[20:21], v[4:7], off offset:256
	s_cbranch_vccz .LBB0_602
	s_waitcnt vmcnt(0)
	v_readlane_b32 s86, v253, 23
	v_readlane_b32 s88, v253, 25
	s_cmpk_gt_u32 s27, 0xff
	v_readlane_b32 s84, v253, 20
	v_readlane_b32 s76, v253, 22
	v_readlane_b32 s87, v253, 24
	v_readlane_b32 s89, v253, 26
	v_readlane_b32 s85, v253, 21
	s_cbranch_scc1 .LBB0_609
	s_barrier
